# router phase: router matrix staged into LDS with sixteen 16-byte loads per thread issued up front (was 2 dwords at a time, 32 exposed round trips)
# speedup vs baseline: 1.0169x; 1.0053x over previous
; #define LAS __attribute__((address_space(3)))
; __device__ __forceinline__ void phase_router(const Args& a, const Ctx& c0, int l, bool last, int skip) {
;     ...
;     LAS float* rl = (LAS float*)c.lds;
;     const float* rt = INP(23) + (size_t)l * DM * NE;
;     for (int i = c.tid; i < DM * NE; i += 512) { const int k = i >> 4, e = i & 15; rl[e * DM + k] = rt[i]; }
;     __syncthreads();
.LBB0_1900:
	s_andn2_b64 vcc, exec, s[2:3]
	s_cbranch_vccnz .LBB0_2081
	v_readlane_b32 s4, v253, 8
	v_readlane_b32 s6, v254, 59
	v_readlane_b32 s5, v253, 9
	v_readlane_b32 s7, v254, 60
	s_and_b64 s[4:5], s[6:7], s[4:5]
	v_readlane_b32 s6, v253, 10
	v_readlane_b32 s7, v253, 11
	s_and_b64 s[6:7], s[4:5], s[6:7]
	s_andn2_b64 vcc, exec, s[6:7]
	v_readlane_b32 s6, v254, 17
	v_readlane_b32 s7, v254, 18
	s_mov_b32 s7, s13
	v_writelane_b32 v254, s6, 17
	s_mov_b64 s[2:3], -1
	s_nop 0
	v_writelane_b32 v254, s7, 18
	s_cbranch_vccz .LBB0_1933
	v_readlane_b32 s8, v254, 21
	v_mov_b32_e32 v2, v0
	v_readlane_b32 s10, v254, 23
	v_readlane_b32 s11, v254, 24
	s_mov_b64 s[2:3], s[10:11]
	v_readfirstlane_b32 s12, v2
	v_cmp_gt_i32_e32 vcc, s83, v2
	v_readlane_b32 s9, v254, 22
	s_and_saveexec_b64 s[6:7], vcc
	s_mov_b64 s[20:21], 0x800
	s_cbranch_execz .LBB0_1915
	v_readlane_b32 s8, v254, 17
	v_readlane_b32 s9, v254, 18
	v_readlane_b32 s14, v254, 19
	v_readlane_b32 s15, v254, 20
	s_lshl_b64 s[8:9], s[8:9], 17
	s_add_u32 s14, s14, s8
	s_addc_u32 s15, s15, s9
	v_lshlrev_b32_e32 v1, 4, v2
	v_and_b32_e32 v3, 3, v2
	v_lshrrev_b32_e32 v4, 2, v2
	v_lshlrev_b32_e32 v3, 15, v3
	v_lshl_add_u32 v3, v4, 2, v3
	global_load_dwordx4 v[16:19], v1, s[14:15]
	v_add_u32_e32 v1, 0x2000, v1
	global_load_dwordx4 v[20:23], v1, s[14:15]
	v_add_u32_e32 v1, 0x2000, v1
	global_load_dwordx4 v[24:27], v1, s[14:15]
	v_add_u32_e32 v1, 0x2000, v1
	global_load_dwordx4 v[28:31], v1, s[14:15]
	v_add_u32_e32 v1, 0x2000, v1
	global_load_dwordx4 v[32:35], v1, s[14:15]
	v_add_u32_e32 v1, 0x2000, v1
	global_load_dwordx4 v[36:39], v1, s[14:15]
	v_add_u32_e32 v1, 0x2000, v1
	global_load_dwordx4 v[40:43], v1, s[14:15]
	v_add_u32_e32 v1, 0x2000, v1
	global_load_dwordx4 v[44:47], v1, s[14:15]
	v_add_u32_e32 v1, 0x2000, v1
	global_load_dwordx4 v[48:51], v1, s[14:15]
	v_add_u32_e32 v1, 0x2000, v1
	global_load_dwordx4 v[52:55], v1, s[14:15]
	v_add_u32_e32 v1, 0x2000, v1
	global_load_dwordx4 v[56:59], v1, s[14:15]
	v_add_u32_e32 v1, 0x2000, v1
	global_load_dwordx4 v[60:63], v1, s[14:15]
	v_add_u32_e32 v1, 0x2000, v1
	global_load_dwordx4 v[64:67], v1, s[14:15]
	v_add_u32_e32 v1, 0x2000, v1
	global_load_dwordx4 v[68:71], v1, s[14:15]
	v_add_u32_e32 v1, 0x2000, v1
	global_load_dwordx4 v[72:75], v1, s[14:15]
	v_add_u32_e32 v1, 0x2000, v1
	global_load_dwordx4 v[76:79], v1, s[14:15]
	s_waitcnt vmcnt(15)
	ds_write_b32 v3, v16
	ds_write_b32 v3, v17 offset:8192
	ds_write_b32 v3, v18 offset:16384
	ds_write_b32 v3, v19 offset:24576
	s_waitcnt vmcnt(14)
	ds_write_b32 v3, v20 offset:512
	ds_write_b32 v3, v21 offset:8704
	ds_write_b32 v3, v22 offset:16896
	ds_write_b32 v3, v23 offset:25088
	s_waitcnt vmcnt(13)
	ds_write_b32 v3, v24 offset:1024
	ds_write_b32 v3, v25 offset:9216
	ds_write_b32 v3, v26 offset:17408
	ds_write_b32 v3, v27 offset:25600
	s_waitcnt vmcnt(12)
	ds_write_b32 v3, v28 offset:1536
	ds_write_b32 v3, v29 offset:9728
	ds_write_b32 v3, v30 offset:17920
	ds_write_b32 v3, v31 offset:26112
	s_waitcnt vmcnt(11)
	ds_write_b32 v3, v32 offset:2048
	ds_write_b32 v3, v33 offset:10240
	ds_write_b32 v3, v34 offset:18432
	ds_write_b32 v3, v35 offset:26624
	s_waitcnt vmcnt(10)
	ds_write_b32 v3, v36 offset:2560
	ds_write_b32 v3, v37 offset:10752
	ds_write_b32 v3, v38 offset:18944
	ds_write_b32 v3, v39 offset:27136
	s_waitcnt vmcnt(9)
	ds_write_b32 v3, v40 offset:3072
	ds_write_b32 v3, v41 offset:11264
	ds_write_b32 v3, v42 offset:19456
	ds_write_b32 v3, v43 offset:27648
	s_waitcnt vmcnt(8)
	ds_write_b32 v3, v44 offset:3584
	ds_write_b32 v3, v45 offset:11776
	ds_write_b32 v3, v46 offset:19968
	ds_write_b32 v3, v47 offset:28160
	s_waitcnt vmcnt(7)
	ds_write_b32 v3, v48 offset:4096
	ds_write_b32 v3, v49 offset:12288
	ds_write_b32 v3, v50 offset:20480
	ds_write_b32 v3, v51 offset:28672
	s_waitcnt vmcnt(6)
	ds_write_b32 v3, v52 offset:4608
	ds_write_b32 v3, v53 offset:12800
	ds_write_b32 v3, v54 offset:20992
	ds_write_b32 v3, v55 offset:29184
	s_waitcnt vmcnt(5)
	ds_write_b32 v3, v56 offset:5120
	ds_write_b32 v3, v57 offset:13312
	ds_write_b32 v3, v58 offset:21504
	ds_write_b32 v3, v59 offset:29696
	s_waitcnt vmcnt(4)
	ds_write_b32 v3, v60 offset:5632
	ds_write_b32 v3, v61 offset:13824
	ds_write_b32 v3, v62 offset:22016
	ds_write_b32 v3, v63 offset:30208
	s_waitcnt vmcnt(3)
	ds_write_b32 v3, v64 offset:6144
	ds_write_b32 v3, v65 offset:14336
	ds_write_b32 v3, v66 offset:22528
	ds_write_b32 v3, v67 offset:30720
	s_waitcnt vmcnt(2)
	ds_write_b32 v3, v68 offset:6656
	ds_write_b32 v3, v69 offset:14848
	ds_write_b32 v3, v70 offset:23040
	ds_write_b32 v3, v71 offset:31232
	s_waitcnt vmcnt(1)
	ds_write_b32 v3, v72 offset:7168
	ds_write_b32 v3, v73 offset:15360
	ds_write_b32 v3, v74 offset:23552
	ds_write_b32 v3, v75 offset:31744
	s_waitcnt vmcnt(0)
	ds_write_b32 v3, v76 offset:7680
	ds_write_b32 v3, v77 offset:15872
	ds_write_b32 v3, v78 offset:24064
	ds_write_b32 v3, v79 offset:32256
	s_waitcnt lgkmcnt(0)
